# LN1+router phase: waves 4-7 start ~7 us later so their loads overlap the first half's compute (single pass per wave otherwise serialises load/compute/store chip-wide)
# baseline (speedup 1.0000x reference)
.LBB0_763:
	v_readlane_b32 s0, v254, 16
	v_readlane_b32 s1, v254, 17
	s_andn2_b64 vcc, exec, s[0:1]
	s_cbranch_vccnz .LBB0_849
	s_mov_b64 s[0:1], s[88:89]
	v_mov_b32_e32 v38, v0
	v_mov_b32_e32 v226, 0x600
	v_mov_b32_e32 v225, 0x42000000
	v_mov_b32_e32 v224, 0xc0a00000
	s_nop 0
	v_readfirstlane_b32 s2, v38
	v_cmp_gt_i32_e64 s[40:41], 16, v38
	v_lshl_add_u32 v1, v38, 2, 0
	s_and_saveexec_b64 s[4:5], s[40:41]
	v_add_u32_e32 v2, 0x25900, v1
	ds_write_b32 v2, v195
	s_or_b64 exec, exec, s[4:5]
	v_readlane_b32 s4, v255, 18
	s_load_dwordx4 s[60:63], s[0:1], 0x58
	s_load_dwordx2 s[6:7], s[0:1], 0x70
	s_nop 0
	s_load_dwordx2 s[0:1], s[0:1], 0x98
	v_readlane_b32 s5, v255, 19
	s_ashr_i32 s5, s4, 31
	v_writelane_b32 v255, s4, 18
	s_ashr_i32 s2, s2, 4
	s_waitcnt vmcnt(0)
	s_and_b32 s2, s2, -4
	v_writelane_b32 v255, s5, 19
	v_readlane_b32 s4, v254, 18
	s_add_i32 s4, s2, s4
	s_cmpk_gt_i32 s4, 0x1fff
	s_waitcnt vmcnt(0) lgkmcnt(0)
	s_barrier
	s_cbranch_scc1 .LBB0_797
	v_readfirstlane_b32 s100, v0
	s_lshr_b32 s100, s100, 8
	s_cmp_eq_u32 s100, 0
	s_cbranch_scc1 .Lp6_stag
	s_sleep 127
	s_sleep 127
.Lp6_stag:
	s_add_u32 s2, s0, 0x8000
	s_addc_u32 s80, s1, 0
	s_add_u32 s64, s0, 0x26300000
	s_addc_u32 s65, s1, 0
	v_readlane_b32 s8, v255, 18
	s_add_u32 s66, s0, 0x68000
	v_readlane_b32 s9, v255, 19
	v_and_b32_e32 v2, 32, v38
	s_addc_u32 s67, s1, 0
	s_lshl_b64 s[68:69], s[8:9], 2
	s_lshl_b32 s8, s8, 1
	v_cmp_eq_u32_e64 s[42:43], 0, v2
	v_and_b32_e32 v2, 16, v38
	s_ashr_i32 s9, s8, 31
	v_cmp_eq_u32_e64 s[44:45], 0, v2
	v_and_b32_e32 v2, 8, v38
	v_and_b32_e32 v39, 63, v38
	s_add_u32 s70, s0, 0x3e700000
	v_cmp_eq_u32_e64 s[46:47], 0, v2
	v_and_b32_e32 v2, 4, v38
	v_lshlrev_b32_e32 v3, 4, v38
	s_addc_u32 s71, s1, 0
	v_and_b32_e32 v4, 64, v218
	v_cmp_eq_u32_e64 s[48:49], 0, v2
	v_lshlrev_b32_e32 v2, 4, v39
	v_and_b32_e32 v40, 48, v3
	v_mov_b32_e32 v3, v195
	v_add_u32_e32 v5, 64, v4
	v_add_u32_e32 v41, 0, v2
	v_lshl_add_u64 v[42:43], s[64:65], 0, v[2:3]
	v_lshl_add_u64 v[44:45], s[70:71], 0, v[2:3]
	v_xor_b32_e32 v2, 32, v218
	v_cmp_lt_i32_e32 vcc, v2, v5
	v_lshrrev_b32_e32 v8, 2, v38
	v_or_b32_e32 v232, v40, v4
	v_cndmask_b32_e32 v2, v218, v2, vcc
	v_lshlrev_b32_e32 v47, 2, v2
	v_xor_b32_e32 v2, 16, v218
	v_cmp_lt_i32_e32 vcc, v2, v5
	v_and_b32_e32 v6, 15, v38
	v_bfe_u32 v7, v38, 2, 2
	v_cndmask_b32_e32 v2, v218, v2, vcc
	v_lshlrev_b32_e32 v49, 2, v2
	v_xor_b32_e32 v2, 8, v218
	v_cmp_lt_i32_e32 vcc, v2, v5
	s_lshl_b64 s[8:9], s[8:9], 13
	s_add_u32 s16, s60, s8
	v_cndmask_b32_e32 v2, v218, v2, vcc
	v_lshlrev_b32_e32 v51, 2, v2
	v_xor_b32_e32 v2, 4, v218
	v_cmp_lt_i32_e32 vcc, v2, v5
	s_addc_u32 s17, s61, s9
	v_lshlrev_b32_e32 v194, 3, v39
	v_cndmask_b32_e32 v2, v218, v2, vcc
	v_lshlrev_b32_e32 v216, 2, v2
	v_xor_b32_e32 v2, 2, v218
	v_cmp_lt_i32_e32 vcc, v2, v5
	s_add_u32 s8, s62, s8
	v_or_b32_e32 v48, 0x400, v194
	v_cndmask_b32_e32 v2, v218, v2, vcc
	v_lshlrev_b32_e32 v217, 2, v2
	v_xor_b32_e32 v2, 1, v218
	v_cmp_lt_i32_e32 vcc, v2, v5
	s_addc_u32 s9, s63, s9
	v_or_b32_e32 v50, 0x600, v194
	v_cndmask_b32_e32 v2, v218, v2, vcc
	v_lshlrev_b32_e32 v231, 2, v2
	v_and_or_b32 v2, v8, 12, v232
	v_lshlrev_b32_e32 v233, 2, v2
	v_bitop3_b32 v2, v38, 1, 15 bitop3:0x6c
	v_cmp_lt_u32_e32 vcc, v2, v6
	v_bitop3_b32 v2, v38, 2, 15 bitop3:0x6c
	v_cmp_gt_u32_e64 s[50:51], 4, v6
	v_cndmask_b32_e64 v234, 0, 1, vcc
	v_cmp_lt_u32_e32 vcc, v2, v6
	v_xor_b32_e32 v2, 3, v218
	v_cmp_eq_u32_e64 s[52:53], 1, v7
	v_cndmask_b32_e64 v235, 0, 1, vcc
	v_cmp_lt_i32_e32 vcc, v2, v5
	v_cmp_eq_u32_e64 s[54:55], 2, v7
	v_cmp_gt_u32_e64 s[56:57], 4, v39
	v_cndmask_b32_e32 v2, v218, v2, vcc
	v_lshlrev_b32_e32 v236, 2, v2
	v_bitop3_b32 v2, v38, 3, 15 bitop3:0x6c
	v_cmp_lt_u32_e32 vcc, v2, v6
	v_xor_b32_e32 v2, 1, v7
	v_or_b32_e32 v46, 0x200, v194
	v_cndmask_b32_e64 v237, 0, 1, vcc
	v_cmp_lt_u32_e32 vcc, v2, v7
	v_xor_b32_e32 v2, 2, v7
	s_nop 0
	v_cndmask_b32_e64 v238, 0, 1, vcc
	v_cmp_lt_u32_e32 vcc, v2, v7
	v_xor_b32_e32 v2, 12, v218
	s_nop 0
	v_cndmask_b32_e64 v239, 0, 1, vcc
	v_cmp_lt_i32_e32 vcc, v2, v5
	s_nop 1
	v_cndmask_b32_e32 v2, v218, v2, vcc
	v_lshlrev_b32_e32 v240, 2, v2
	v_xor_b32_e32 v2, 3, v7
	v_cmp_lt_u32_e32 vcc, v2, v7
	v_lshlrev_b32_e32 v2, 5, v39
	v_lshl_add_u64 v[52:53], s[16:17], 0, v[2:3]
	v_lshl_add_u64 v[54:55], s[8:9], 0, v[2:3]
	v_lshlrev_b32_e32 v2, 2, v48
	v_lshl_add_u64 v[56:57], s[16:17], 0, v[2:3]
	v_lshl_add_u64 v[58:59], s[8:9], 0, v[2:3]
	v_lshlrev_b32_e32 v2, 2, v50
	v_lshl_add_u64 v[60:61], s[16:17], 0, v[2:3]
	v_lshl_add_u64 v[62:63], s[8:9], 0, v[2:3]
	v_lshlrev_b32_e32 v2, 2, v6
	v_lshl_add_u64 v[64:65], s[6:7], 0, v[2:3]
	v_lshl_add_u64 v[2:3], s[0:1], 0, v[194:195]
	s_mov_b64 s[6:7], 0x2c300000
	v_cndmask_b32_e64 v241, 0, 1, vcc
	v_lshl_add_u64 v[66:67], v[2:3], 0, s[6:7]
	s_branch .LBB0_769
